# v44 + DSA P*V step V^T fragments via ds_read_b64_tr_b16 pairs, reads pipelined one block ahead
# speedup vs baseline: 1.0001x; 1.0001x over previous
.LBB0_1123:
	s_or_b64 exec, exec, s[2:3]
	s_waitcnt lgkmcnt(0)
	v_add_u32_e32 v2, 31, v172
	v_and_b32_e32 v173, 15, v151
	v_ashrrev_i32_e32 v174, 4, v151
	v_ashrrev_i32_e32 v176, 5, v2
	v_mov_b32_e32 v29, 0
	v_lshlrev_b32_e32 v148, 7, v173
	v_mov_b32_e32 v149, v147
	v_cmp_lt_i32_e32 vcc, 0, v176
	v_lshlrev_b32_e32 v150, 2, v174
	v_mov_b32_e32 v28, v29
	v_mov_b32_e32 v27, v29
	v_mov_b32_e32 v26, v29
	v_mov_b32_e32 v33, v29
	v_mov_b32_e32 v32, v29
	v_mov_b32_e32 v31, v29
	v_mov_b32_e32 v30, v29
	v_mov_b32_e32 v25, v29
	v_mov_b32_e32 v24, v29
	v_mov_b32_e32 v23, v29
	v_mov_b32_e32 v22, v29
	v_mov_b32_e32 v21, v29
	v_mov_b32_e32 v20, v29
	v_mov_b32_e32 v19, v29
	v_mov_b32_e32 v18, v29
	v_mov_b32_e32 v17, v29
	v_mov_b32_e32 v16, v29
	v_mov_b32_e32 v15, v29
	v_mov_b32_e32 v14, v29
	v_mov_b32_e32 v13, v29
	v_mov_b32_e32 v12, v29
	v_mov_b32_e32 v11, v29
	v_mov_b32_e32 v10, v29
	v_mov_b32_e32 v9, v29
	v_mov_b32_e32 v8, v29
	v_mov_b32_e32 v7, v29
	v_mov_b32_e32 v6, v29
	v_mov_b32_e32 v5, v29
	v_mov_b32_e32 v4, v29
	v_mov_b32_e32 v3, v29
	v_mov_b32_e32 v2, v29
	v_mov_b32_e32 v179, v29
	s_and_saveexec_b64 s[0:1], vcc
	s_cbranch_execz .LBB0_1127
	s_mul_i32 s2, s97, 0x3400
	s_mul_hi_u32 s3, s96, 0x3400
	s_add_i32 s3, s3, s2
	s_mul_i32 s2, s96, 0x3400
	s_add_u32 s2, s82, s2
	v_lshlrev_b32_e32 v4, 3, v174
	s_addc_u32 s3, s83, s3
	v_lshlrev_b32_e32 v146, 1, v148
	v_ashrrev_i32_e32 v5, 31, v4
	v_lshl_add_u64 v[2:3], s[2:3], 0, v[146:147]
	v_lshlrev_b64 v[152:153], 1, v[4:5]
	v_lshl_add_u64 v[2:3], v[2:3], 0, v[152:153]
	s_mov_b64 s[2:3], 0x1800
	v_lshl_add_u64 v[4:5], v[2:3], 0, s[2:3]
	v_add_co_u32_e32 v2, vcc, s33, v2
	v_add_u32_e32 v10, s89, v150
	s_nop 0
	v_addc_co_u32_e32 v3, vcc, 0, v3, vcc
	global_load_dwordx4 v[34:37], v[4:5], off offset:64
	global_load_dwordx4 v[38:41], v[4:5], off offset:128
	global_load_dwordx4 v[42:45], v[2:3], off offset:2048
	global_load_dwordx4 v[46:49], v[4:5], off offset:192
	ds_read2_b32 v[2:3], v10 offset0:24 offset1:28
	s_mul_i32 s5, s78, 0x3400000
	s_mul_hi_i32 s4, s78, 0x3400000
	s_add_u32 s2, s82, s5
	s_addc_u32 s3, s83, s4
	v_mov_b64_e32 v[4:5], s[2:3]
	s_waitcnt lgkmcnt(0)
	v_mad_i64_i32 v[6:7], s[4:5], v3, s35, v[4:5]
	v_lshlrev_b32_e32 v146, 4, v173
	v_lshl_add_u64 v[6:7], v[6:7], 0, v[146:147]
	ds_read2_b32 v[8:9], v10 offset0:16 offset1:20
	v_add_co_u32_e32 v6, vcc, s41, v6
	v_mad_i64_i32 v[2:3], s[4:5], v2, s35, v[4:5]
	s_nop 0
	v_addc_co_u32_e32 v7, vcc, 0, v7, vcc
	v_lshl_add_u64 v[2:3], v[2:3], 0, v[146:147]
	v_add_co_u32_e32 v2, vcc, s41, v2
	v_mov_b32_e32 v179, 0
	s_nop 0
	v_addc_co_u32_e32 v3, vcc, 0, v3, vcc
	global_load_dwordx4 v[54:57], v[6:7], off offset:2304
	global_load_dwordx4 v[50:53], v[2:3], off offset:2304
	s_waitcnt lgkmcnt(0)
	v_mad_i64_i32 v[2:3], s[4:5], v9, s35, v[4:5]
	v_lshl_add_u64 v[2:3], v[2:3], 0, v[146:147]
	v_mad_i64_i32 v[6:7], s[4:5], v8, s35, v[4:5]
	ds_read2_b32 v[8:9], v10 offset0:8 offset1:12
	v_add_co_u32_e32 v2, vcc, s41, v2
	v_lshl_add_u64 v[6:7], v[6:7], 0, v[146:147]
	s_nop 0
	v_addc_co_u32_e32 v3, vcc, 0, v3, vcc
	v_add_co_u32_e32 v6, vcc, s41, v6
	s_mov_b32 s7, 0
	s_nop 0
	v_addc_co_u32_e32 v7, vcc, 0, v7, vcc
	global_load_dwordx4 v[62:65], v[2:3], off offset:2304
	global_load_dwordx4 v[58:61], v[6:7], off offset:2304
	ds_read2_b32 v[2:3], v10 offset1:4
	s_waitcnt lgkmcnt(1)
	v_mad_i64_i32 v[6:7], s[4:5], v9, s35, v[4:5]
	v_lshl_add_u64 v[6:7], v[6:7], 0, v[146:147]
	v_add_co_u32_e32 v6, vcc, s41, v6
	v_mad_i64_i32 v[8:9], s[4:5], v8, s35, v[4:5]
	s_nop 0
	v_addc_co_u32_e32 v7, vcc, 0, v7, vcc
	v_lshl_add_u64 v[8:9], v[8:9], 0, v[146:147]
	v_add_co_u32_e32 v8, vcc, s41, v8
	v_mov_b32_e32 v181, 0xf149f2ca
	s_nop 0
	v_addc_co_u32_e32 v9, vcc, 0, v9, vcc
	global_load_dwordx4 v[70:73], v[6:7], off offset:2304
	global_load_dwordx4 v[66:69], v[8:9], off offset:2304
	s_waitcnt lgkmcnt(0)
	v_mad_i64_i32 v[6:7], s[4:5], v3, s35, v[4:5]
	v_lshl_add_u32 v8, v173, 2, s89
	v_lshl_add_u64 v[6:7], v[6:7], 0, v[146:147]
	ds_read2_b32 v[8:9], v8 offset1:16
	v_add_co_u32_e32 v6, vcc, s41, v6
	v_mad_i64_i32 v[2:3], s[4:5], v2, s35, v[4:5]
	s_nop 0
	v_addc_co_u32_e32 v7, vcc, 0, v7, vcc
	v_lshl_add_u64 v[2:3], v[2:3], 0, v[146:147]
	v_add_co_u32_e32 v2, vcc, s41, v2
	s_mov_b32 s6, 0
	s_nop 0
	v_addc_co_u32_e32 v3, vcc, 0, v3, vcc
	global_load_dwordx4 v[78:81], v[6:7], off offset:2304
	global_load_dwordx4 v[74:77], v[2:3], off offset:2304
	s_waitcnt lgkmcnt(0)
	v_mad_i64_i32 v[2:3], s[4:5], v9, s35, v[4:5]
	v_mad_i64_i32 v[4:5], s[4:5], v8, s35, v[4:5]
	v_lshl_add_u64 v[4:5], v[4:5], 0, v[152:153]
	v_lshl_add_u64 v[2:3], v[2:3], 0, v[152:153]
	v_lshl_add_u64 v[8:9], v[4:5], 0, s[94:95]
	v_lshl_add_u64 v[6:7], v[2:3], 0, s[94:95]
	global_load_dwordx4 v[82:85], v[8:9], off offset:192
	global_load_dwordx4 v[86:89], v[8:9], off offset:128
	global_load_dwordx4 v[90:93], v[6:7], off offset:128
	global_load_dwordx4 v[102:105], v[6:7], off offset:64
	global_load_dwordx4 v[98:101], v[6:7], off offset:192
	global_load_dwordx4 v[94:97], v[8:9], off offset:64
	v_add_co_u32_e32 v2, vcc, s41, v2
	s_movk_i32 s4, 0x120
	s_nop 0
	v_addc_co_u32_e32 v3, vcc, 0, v3, vcc
	v_add_co_u32_e32 v4, vcc, s41, v4
	v_mov_b32_e32 v7, v179
	s_nop 0
	v_addc_co_u32_e32 v5, vcc, 0, v5, vcc
	global_load_dwordx4 v[106:109], v[2:3], off offset:2048
	global_load_dwordx4 v[110:113], v[4:5], off offset:2048
	v_mul_lo_u32 v5, v174, s4
	s_movk_i32 s4, 0x480
	v_lshlrev_b32_e32 v2, 3, v173
	v_add_u32_e32 v3, s89, v146
	v_lshlrev_b32_e32 v4, 1, v173
	v_mul_lo_u32 v6, v174, s4
	v_add3_u32 v177, s89, v4, v6
	v_lshrrev_b32_e32 v243, 2, v173
	v_mul_u32_u24_e32 v243, 0x120, v243
	v_and_b32_e32 v244, 3, v173
	v_lshl_add_u32 v243, v244, 3, v243
	v_mul_u32_u24_e32 v244, 0x480, v174
	v_add3_u32 v243, v243, v244, s89
	v_add_u32_e32 v243, 0x400, v243
	s_mov_b64 s[4:5], 0
	v_add_u32_e32 v178, v3, v5
	v_lshlrev_b32_e32 v146, 1, v2
	v_mov_b32_e32 v2, 0
	v_mov_b32_e32 v3, v179
	v_mov_b32_e32 v4, v179
	v_mov_b32_e32 v5, v179
	v_mov_b32_e32 v6, 0
	v_mov_b32_e32 v8, v179
	v_mov_b32_e32 v9, v179
	v_mov_b32_e32 v10, 0
	v_mov_b32_e32 v11, v179
	v_mov_b32_e32 v12, v179
	v_mov_b32_e32 v13, v179
	v_mov_b32_e32 v14, 0
	v_mov_b32_e32 v15, v179
	v_mov_b32_e32 v16, v179
	v_mov_b32_e32 v17, v179
	v_mov_b32_e32 v18, 0
	v_mov_b32_e32 v19, v179
	v_mov_b32_e32 v20, v179
	v_mov_b32_e32 v21, v179
	v_mov_b32_e32 v22, 0
	v_mov_b32_e32 v23, v179
	v_mov_b32_e32 v24, v179
	v_mov_b32_e32 v25, v179
	v_mov_b32_e32 v30, 0
	v_mov_b32_e32 v31, v179
	v_mov_b32_e32 v32, v179
	v_mov_b32_e32 v33, v179
	v_mov_b32_e32 v26, 0
	v_mov_b32_e32 v27, v179
	v_mov_b32_e32 v28, v179
	v_mov_b32_e32 v29, v179
.LBB0_1125:
	s_add_i32 s6, s6, 1
	s_add_i32 s8, s7, 32
	s_waitcnt vmcnt(7)
	ds_write_b128 v178, v[74:77] offset:1024
	s_waitcnt vmcnt(6)
	ds_write_b128 v178, v[78:81] offset:2176
	s_waitcnt vmcnt(5)
	ds_write_b128 v178, v[66:69] offset:3328
	s_waitcnt vmcnt(4)
	ds_write_b128 v178, v[70:73] offset:4480
	s_waitcnt vmcnt(3)
	ds_write_b128 v178, v[58:61] offset:5632
	s_waitcnt vmcnt(2)
	ds_write_b128 v178, v[62:65] offset:6784
	s_waitcnt vmcnt(1)
	ds_write_b128 v178, v[50:53] offset:7936
	s_waitcnt vmcnt(0)
	ds_write_b128 v178, v[54:57] offset:9088
	v_cmp_lt_i32_e32 vcc, s6, v176
	v_mov_b32_e32 v50, s7
	v_mov_b32_e32 v51, s8
	v_cndmask_b32_e32 v50, v50, v51, vcc
	v_lshl_add_u32 v52, v50, 2, s89
	v_lshl_add_u32 v50, v173, 2, v52
	ds_read2_b32 v[50:51], v50 offset1:16
	v_lshl_add_u32 v58, v174, 2, v52
	v_mov_b64_e32 v[186:187], s[2:3]
	ds_read2_b32 v[52:53], v58 offset1:4
	ds_read2_b32 v[54:55], v58 offset0:8 offset1:12
	ds_read2_b32 v[56:57], v58 offset0:16 offset1:20
	ds_read2_b32 v[184:185], v58 offset0:24 offset1:28
	s_waitcnt vmcnt(0)
	v_mfma_f32_16x16x32_bf16 v[110:113], v[110:113], v[42:45], 0
	s_waitcnt lgkmcnt(4)
	v_mad_i64_i32 v[58:59], s[10:11], v50, s35, v[186:187]
	v_lshl_add_u64 v[58:59], v[58:59], 0, v[152:153]
	v_lshl_add_u64 v[60:61], v[58:59], 0, s[94:95]
	v_mad_i64_i32 v[50:51], s[10:11], v51, s35, v[186:187]
	v_add_co_u32_e32 v58, vcc, s41, v58
	v_lshl_add_u64 v[50:51], v[50:51], 0, v[152:153]
	s_nop 0
	v_addc_co_u32_e32 v59, vcc, 0, v59, vcc
	v_lshl_add_u64 v[62:63], v[50:51], 0, s[94:95]
	v_add_co_u32_e32 v50, vcc, s41, v50
	global_load_dwordx4 v[118:121], v[58:59], off offset:2048
	s_nop 0
	v_addc_co_u32_e32 v51, vcc, 0, v51, vcc
	global_load_dwordx4 v[114:117], v[50:51], off offset:2048
	global_load_dwordx4 v[134:137], v[60:61], off offset:64
	global_load_dwordx4 v[122:125], v[62:63], off offset:64
	global_load_dwordx4 v[138:141], v[60:61], off offset:128
	global_load_dwordx4 v[126:129], v[62:63], off offset:128
	global_load_dwordx4 v[142:145], v[60:61], off offset:192
	global_load_dwordx4 v[130:133], v[62:63], off offset:192
	s_waitcnt lgkmcnt(3)
	v_mad_i64_i32 v[50:51], s[10:11], v52, s35, v[186:187]
	v_lshl_add_u64 v[50:51], v[50:51], 0, v[146:147]
	v_add_co_u32_e32 v50, vcc, s41, v50
	v_mfma_f32_16x16x32_bf16 v[106:109], v[106:109], v[42:45], 0
	s_nop 0
	v_addc_co_u32_e32 v51, vcc, 0, v51, vcc
	global_load_dwordx4 v[74:77], v[50:51], off offset:2304
	v_mad_i64_i32 v[50:51], s[10:11], v53, s35, v[186:187]
	v_lshl_add_u64 v[50:51], v[50:51], 0, v[146:147]
	v_add_co_u32_e32 v50, vcc, s41, v50
	v_mfma_f32_16x16x32_bf16 v[94:97], v[94:97], v[34:37], v[110:113]
	s_nop 0
	v_addc_co_u32_e32 v51, vcc, 0, v51, vcc
	global_load_dwordx4 v[78:81], v[50:51], off offset:2304
	s_waitcnt lgkmcnt(2)
	v_mad_i64_i32 v[50:51], s[10:11], v54, s35, v[186:187]
	v_lshl_add_u64 v[50:51], v[50:51], 0, v[146:147]
	v_add_co_u32_e32 v50, vcc, s41, v50
	v_mfma_f32_16x16x32_bf16 v[102:105], v[102:105], v[34:37], v[106:109]
	s_nop 0
	v_addc_co_u32_e32 v51, vcc, 0, v51, vcc
	global_load_dwordx4 v[66:69], v[50:51], off offset:2304
	v_mad_i64_i32 v[50:51], s[10:11], v55, s35, v[186:187]
	v_lshl_add_u64 v[50:51], v[50:51], 0, v[146:147]
	v_add_co_u32_e32 v50, vcc, s41, v50
	v_mfma_f32_16x16x32_bf16 v[86:89], v[86:89], v[38:41], v[94:97]
	s_nop 0
	v_addc_co_u32_e32 v51, vcc, 0, v51, vcc
	global_load_dwordx4 v[70:73], v[50:51], off offset:2304
	s_waitcnt lgkmcnt(1)
	v_mad_i64_i32 v[50:51], s[10:11], v56, s35, v[186:187]
	v_lshl_add_u64 v[50:51], v[50:51], 0, v[146:147]
	v_add_co_u32_e32 v50, vcc, s41, v50
	v_mfma_f32_16x16x32_bf16 v[90:93], v[90:93], v[38:41], v[102:105]
	s_nop 0
	v_addc_co_u32_e32 v51, vcc, 0, v51, vcc
	global_load_dwordx4 v[58:61], v[50:51], off offset:2304
	v_mad_i64_i32 v[50:51], s[10:11], v57, s35, v[186:187]
	v_lshl_add_u64 v[50:51], v[50:51], 0, v[146:147]
	v_add_co_u32_e32 v50, vcc, s41, v50
	s_waitcnt lgkmcnt(0)
	v_mad_i64_i32 v[54:55], s[10:11], v185, s35, v[186:187]
	v_addc_co_u32_e32 v51, vcc, 0, v51, vcc
	global_load_dwordx4 v[62:65], v[50:51], off offset:2304
	v_mad_i64_i32 v[50:51], s[10:11], v184, s35, v[186:187]
	v_lshl_add_u64 v[50:51], v[50:51], 0, v[146:147]
	v_add_co_u32_e32 v50, vcc, s41, v50
	v_mfma_f32_16x16x32_bf16 v[82:85], v[82:85], v[46:49], v[86:89]
	s_nop 0
	v_addc_co_u32_e32 v51, vcc, 0, v51, vcc
	v_lshl_add_u64 v[54:55], v[54:55], 0, v[146:147]
	v_mfma_f32_16x16x32_bf16 v[86:89], v[98:101], v[46:49], v[90:93]
	v_add_co_u32_e32 v54, vcc, s41, v54
	s_nop 2
	v_mul_f32_e32 v82, 0x3e0293ee, v82
	v_addc_co_u32_e32 v55, vcc, 0, v55, vcc
	v_add_u32_e32 v90, s7, v150
	v_add_u32_e32 v91, 16, v90
	v_cmp_lt_i32_e32 vcc, v90, v172
	v_mul_f32_e32 v86, 0x3e0293ee, v86
	v_add_u32_e32 v92, 1, v90
	v_cndmask_b32_e32 v82, v170, v82, vcc
	v_cmp_lt_i32_e32 vcc, v91, v172
	v_add_u32_e32 v93, 17, v90
	v_mul_f32_e32 v83, 0x3e0293ee, v83
	v_cndmask_b32_e32 v86, v170, v86, vcc
	v_cmp_lt_i32_e32 vcc, v92, v172
	v_max_f32_e32 v91, v82, v86
	s_mov_b32 s7, 0xff800000
	v_cndmask_b32_e32 v92, v170, v83, vcc
	v_cmp_lt_i32_e32 vcc, v93, v172
	v_mul_f32_e32 v83, 0x3e0293ee, v87
	v_add_u32_e32 v93, 18, v90
	v_cndmask_b32_e32 v87, v170, v83, vcc
	v_max_f32_e32 v83, v92, v87
	v_max3_f32 v83, v91, s7, v83
	v_add_u32_e32 v91, 2, v90
	v_cmp_lt_i32_e32 vcc, v91, v172
	v_mul_f32_e32 v84, 0x3e0293ee, v84
	v_mul_f32_e32 v85, 0x3e0293ee, v85
	v_cndmask_b32_e32 v91, v170, v84, vcc
	v_cmp_lt_i32_e32 vcc, v93, v172
	v_mul_f32_e32 v84, 0x3e0293ee, v88
	v_add_u32_e32 v93, 3, v90
	v_cndmask_b32_e32 v88, v170, v84, vcc
	v_add_u32_e32 v90, 19, v90
	v_cmp_lt_i32_e32 vcc, v93, v172
	v_max_f32_e32 v84, v91, v88
	global_load_dwordx4 v[50:53], v[50:51], off offset:2304
	v_cndmask_b32_e32 v93, v170, v85, vcc
	v_cmp_lt_i32_e32 vcc, v90, v172
	v_mul_f32_e32 v85, 0x3e0293ee, v89
	global_load_dwordx4 v[54:57], v[54:55], off offset:2304
	v_cndmask_b32_e32 v90, v170, v85, vcc
	v_max_f32_e32 v85, v93, v90
	v_max3_f32 v83, v83, v84, v85
	ds_bpermute_b32 v84, v161, v83
	v_mov_b32_e32 v85, v147
	v_mov_b32_e32 v182, v179
	v_cmp_eq_u32_e32 vcc, s6, v176
	s_waitcnt vmcnt(15)
	v_mov_b64_e32 v[110:111], v[118:119]
	s_waitcnt lgkmcnt(0)
	v_max_f32_e32 v84, v84, v84
	v_max_f32_e32 v83, v83, v84
	ds_bpermute_b32 v84, v162, v83
	s_waitcnt vmcnt(14)
	v_mov_b64_e32 v[106:107], v[114:115]
	s_waitcnt vmcnt(12)
	v_mov_b64_e32 v[102:103], v[122:123]
	s_waitcnt vmcnt(8)
	v_mov_b64_e32 v[98:99], v[130:131]
	s_or_b64 s[4:5], vcc, s[4:5]
	s_waitcnt lgkmcnt(0)
	v_max3_f32 v180, v181, v83, v84
	v_sub_f32_e32 v82, v82, v180
	v_exp_f32_e32 v95, v82
	v_sub_f32_e32 v82, v86, v180
	v_exp_f32_e32 v96, v82
	v_sub_f32_e32 v82, v92, v180
	v_sub_f32_e32 v84, v87, v180
	v_exp_f32_e32 v82, v82
	v_exp_f32_e32 v84, v84
	v_add_f32_e32 v83, v95, v96
	v_sub_f32_e32 v94, v181, v180
	s_mov_b32 s7, s8
	v_pk_add_f32 v[86:87], v[82:83], v[84:85]
	v_sub_f32_e32 v83, v91, v180
	v_pk_add_f32 v[86:87], v[86:87], v[86:87] op_sel_hi:[0,1]
	v_sub_f32_e32 v85, v88, v180
	v_sub_f32_e32 v86, v93, v180
	v_exp_f32_e32 v83, v83
	v_exp_f32_e32 v85, v85
	v_exp_f32_e32 v88, v86
	v_sub_f32_e32 v86, v90, v180
	v_exp_f32_e32 v86, v86
	v_add_f32_e32 v89, v83, v85
	v_cvt_pk_bf16_f32 v82, v95, v82
	v_cvt_pk_bf16_f32 v83, v83, v88
	v_pk_add_f32 v[90:91], v[88:89], v[86:87]
	v_cvt_pk_bf16_f32 v84, v96, v84
	v_cvt_pk_bf16_f32 v85, v85, v86
	s_waitcnt lgkmcnt(0)
	v_mov_b64_e32 v[112:113], v[120:121]
	v_add_f32_e32 v87, v90, v91
	ds_bpermute_b32 v89, v161, v87
	v_exp_f32_e32 v90, v94
	v_mov_b64_e32 v[108:109], v[116:117]
	v_mov_b64_e32 v[104:105], v[124:125]
	v_mov_b64_e32 v[100:101], v[132:133]
	s_waitcnt lgkmcnt(0)
	v_add_f32_e32 v87, v87, v89
	ds_bpermute_b32 v89, v162, v87
	v_pk_mul_f32 v[4:5], v[4:5], v[90:91] op_sel_hi:[1,0]
	v_pk_mul_f32 v[2:3], v[2:3], v[90:91] op_sel_hi:[1,0]
	v_pk_mul_f32 v[8:9], v[8:9], v[90:91] op_sel_hi:[1,0]
	v_pk_mul_f32 v[6:7], v[6:7], v[90:91] op_sel_hi:[1,0]
	v_pk_mul_f32 v[12:13], v[12:13], v[90:91] op_sel_hi:[1,0]
	v_pk_mul_f32 v[10:11], v[10:11], v[90:91] op_sel_hi:[1,0]
	v_pk_mul_f32 v[16:17], v[16:17], v[90:91] op_sel_hi:[1,0]
	v_pk_mul_f32 v[14:15], v[14:15], v[90:91] op_sel_hi:[1,0]
	v_pk_mul_f32 v[20:21], v[20:21], v[90:91] op_sel_hi:[1,0]
	v_pk_mul_f32 v[18:19], v[18:19], v[90:91] op_sel_hi:[1,0]
	v_pk_mul_f32 v[24:25], v[24:25], v[90:91] op_sel_hi:[1,0]
	v_pk_mul_f32 v[22:23], v[22:23], v[90:91] op_sel_hi:[1,0]
	v_pk_mul_f32 v[32:33], v[32:33], v[90:91] op_sel_hi:[1,0]
	v_pk_mul_f32 v[30:31], v[30:31], v[90:91] op_sel_hi:[1,0]
	v_pk_mul_f32 v[28:29], v[28:29], v[90:91] op_sel_hi:[1,0]
	v_pk_mul_f32 v[26:27], v[26:27], v[90:91] op_sel_hi:[1,0]
	s_waitcnt lgkmcnt(0)
	v_add_f32_e32 v179, v87, v89
	ds_read_b64_tr_b16 v[86:87], v243
	ds_read_b64_tr_b16 v[88:89], v243 offset:4608
	ds_read_b64_tr_b16 v[244:245], v243 offset:32
	ds_read_b64_tr_b16 v[246:247], v243 offset:4640
	v_fmac_f32_e32 v179, v182, v90
	v_mov_b32_e32 v181, v180
	s_waitcnt lgkmcnt(2)
	v_mfma_f32_16x16x32_bf16 v[2:5], v[86:89], v[82:85], v[2:5]
	ds_read_b64_tr_b16 v[86:87], v243 offset:64
	ds_read_b64_tr_b16 v[88:89], v243 offset:4672
	s_waitcnt lgkmcnt(2)
	v_mfma_f32_16x16x32_bf16 v[6:9], v[244:247], v[82:85], v[6:9]
	ds_read_b64_tr_b16 v[244:245], v243 offset:96
	ds_read_b64_tr_b16 v[246:247], v243 offset:4704
	s_waitcnt lgkmcnt(2)
	v_mfma_f32_16x16x32_bf16 v[10:13], v[86:89], v[82:85], v[10:13]
	ds_read_b64_tr_b16 v[86:87], v243 offset:128
	ds_read_b64_tr_b16 v[88:89], v243 offset:4736
	s_waitcnt lgkmcnt(2)
	v_mfma_f32_16x16x32_bf16 v[14:17], v[244:247], v[82:85], v[14:17]
	ds_read_b64_tr_b16 v[244:245], v243 offset:160
	ds_read_b64_tr_b16 v[246:247], v243 offset:4768
	s_waitcnt lgkmcnt(2)
	v_mfma_f32_16x16x32_bf16 v[18:21], v[86:89], v[82:85], v[18:21]
	ds_read_b64_tr_b16 v[86:87], v243 offset:192
	ds_read_b64_tr_b16 v[88:89], v243 offset:4800
	s_waitcnt lgkmcnt(2)
	v_mfma_f32_16x16x32_bf16 v[22:25], v[244:247], v[82:85], v[22:25]
	ds_read_b64_tr_b16 v[244:245], v243 offset:224
	ds_read_b64_tr_b16 v[246:247], v243 offset:4832
	s_waitcnt lgkmcnt(2)
	v_mfma_f32_16x16x32_bf16 v[30:33], v[86:89], v[82:85], v[30:33]
	v_mov_b64_e32 v[94:95], v[134:135]
	v_mov_b64_e32 v[90:91], v[126:127]
	s_waitcnt lgkmcnt(0)
	v_mfma_f32_16x16x32_bf16 v[26:29], v[244:247], v[82:85], v[26:29]
	v_mov_b64_e32 v[86:87], v[138:139]
	v_mov_b64_e32 v[82:83], v[142:143]
	v_mov_b64_e32 v[96:97], v[136:137]
	v_mov_b64_e32 v[88:89], v[140:141]
	v_mov_b64_e32 v[84:85], v[144:145]
	v_mov_b64_e32 v[92:93], v[128:129]
	s_andn2_b64 exec, exec, s[4:5]
	s_cbranch_execnz .LBB0_1125
	s_or_b64 exec, exec, s[4:5]

	.amdhsa_kernel _Z10fwd_kernel4Args
		.amdhsa_group_segment_fixed_size 0
		.amdhsa_private_segment_fixed_size 0
		.amdhsa_kernarg_size 392
		.amdhsa_user_sgpr_count 2
		.amdhsa_user_sgpr_dispatch_ptr 0
		.amdhsa_user_sgpr_queue_ptr 0
		.amdhsa_user_sgpr_kernarg_segment_ptr 1
		.amdhsa_user_sgpr_dispatch_id 0
		.amdhsa_user_sgpr_kernarg_preload_length 0
		.amdhsa_user_sgpr_kernarg_preload_offset 0
		.amdhsa_user_sgpr_private_segment_size 0
		.amdhsa_uses_dynamic_stack 0
		.amdhsa_enable_private_segment 0
		.amdhsa_system_sgpr_workgroup_id_x 1
		.amdhsa_system_sgpr_workgroup_id_y 0
		.amdhsa_system_sgpr_workgroup_id_z 0
		.amdhsa_system_sgpr_workgroup_info 0
		.amdhsa_system_vgpr_workitem_id 0
		.amdhsa_next_free_vgpr 248
		.amdhsa_next_free_sgpr 98
		.amdhsa_accum_offset 248
		.amdhsa_reserve_vcc 1
		.amdhsa_float_round_mode_32 0
		.amdhsa_float_round_mode_16_64 0
		.amdhsa_float_denorm_mode_32 3
		.amdhsa_float_denorm_mode_16_64 3
		.amdhsa_dx10_clamp 1
		.amdhsa_ieee_mode 1
		.amdhsa_fp16_overflow 0
		.amdhsa_tg_split 0
		.amdhsa_exception_fp_ieee_invalid_op 0
		.amdhsa_exception_fp_denorm_src 0
		.amdhsa_exception_fp_ieee_div_zero 0
		.amdhsa_exception_fp_ieee_overflow 0
		.amdhsa_exception_fp_ieee_underflow 0
		.amdhsa_exception_fp_ieee_inexact 0
		.amdhsa_exception_int_div_zero 0
	.end_amdhsa_kernel

amdhsa.kernels:
  - .agpr_count:     0
    .args:
      - .offset:         0
        .size:           136
        .value_kind:     by_value
      - .offset:         136
        .size:           4
        .value_kind:     hidden_block_count_x
      - .offset:         140
        .size:           4
        .value_kind:     hidden_block_count_y
      - .offset:         144
        .size:           4
        .value_kind:     hidden_block_count_z
      - .offset:         148
        .size:           2
        .value_kind:     hidden_group_size_x
      - .offset:         150
        .size:           2
        .value_kind:     hidden_group_size_y
      - .offset:         152
        .size:           2
        .value_kind:     hidden_group_size_z
      - .offset:         154
        .size:           2
        .value_kind:     hidden_remainder_x
      - .offset:         156
        .size:           2
        .value_kind:     hidden_remainder_y
      - .offset:         158
        .size:           2
        .value_kind:     hidden_remainder_z
      - .offset:         176
        .size:           8
        .value_kind:     hidden_global_offset_x
      - .offset:         184
        .size:           8
        .value_kind:     hidden_global_offset_y
      - .offset:         192
        .size:           8
        .value_kind:     hidden_global_offset_z
      - .offset:         200
        .size:           2
        .value_kind:     hidden_grid_dims
      - .offset:         256
        .size:           4
        .value_kind:     hidden_dynamic_lds_size
    .group_segment_fixed_size: 0
    .kernarg_segment_align: 8
    .kernarg_segment_size: 392
    .language:       OpenCL C
    .language_version:
      - 2
      - 0
    .max_flat_workgroup_size: 512
    .name:           _Z10fwd_kernel4Args
    .private_segment_fixed_size: 0
    .sgpr_count:     104
    .sgpr_spill_count: 61
    .symbol:         _Z10fwd_kernel4Args.kd
    .uniform_work_group_size: 1
    .uses_dynamic_stack: false
    .vgpr_count:     248
    .vgpr_spill_count: 0
    .wavefront_size: 64
